# barrier v2: last XCD leader bumps every XCD generation word directly, other leaders wait on their own word
# baseline (speedup 1.0000x reference)
; __device__ __forceinline__ unsigned xb_ld(unsigned* p)              { return __hip_atomic_load(p, __ATOMIC_RELAXED, __HIP_MEMORY_SCOPE_AGENT); }
; __device__ __forceinline__ unsigned xb_add(unsigned* p, unsigned v) { return __hip_atomic_fetch_add(p, v, __ATOMIC_RELAXED, __HIP_MEMORY_SCOPE_AGENT); }
; #define XB_SPIN(cond, bar) do { unsigned _sp = 0; while (cond) { __builtin_amdgcn_s_sleep(1); \
;     if ((++_sp & 255u) == 0u) { if (xb_ld(&(bar)[XB_TMO])) break; if (_sp > XB_SPIN_CAP) { atomicAdd(&(bar)[XB_TMO], 1u); break; } } } } while (0)
; __device__ __forceinline__ void xcd_barrier(const XcdBarrier& b) {
;     ...
;         const unsigned old = xb_add(&bar[XB_XSUB(b.x)], 1u);
;         const unsigned gen = old / nloc;
;         if (old + 1u == (gen + 1u) * nloc) {
;             __builtin_amdgcn_fence(__ATOMIC_RELEASE, "agent");
;             asm volatile("s_waitcnt vmcnt(0)" ::: "memory");
;             const unsigned og = xb_add(&bar[XB_TOP], 1u);
;             const unsigned tg = og / nx;
;             if (og + 1u == (tg + 1u) * nx) xb_add(&bar[XB_TOPGEN], 1u);
;             else XB_SPIN(xb_ld(&bar[XB_TOPGEN]) == tg, bar);
;             __builtin_amdgcn_fence(__ATOMIC_ACQUIRE, "agent");
;             xb_add(&bar[XB_XGEN(b.x)], 1u);
;             asm volatile("s_waitcnt vmcnt(0)" ::: "memory");
;         } else {
;             XB_SPIN(xb_ld(&bar[XB_XGEN(b.x)]) == gen, bar);
;             __builtin_amdgcn_fence(__ATOMIC_ACQUIRE, "agent");
;             asm volatile("s_waitcnt vmcnt(0)" ::: "memory");
;         }
.Lgb0_leader:
	buffer_wbl2 sc1
	v_mov_b32_e32 v3, v5
	s_add_u32 s4, s64, 0x3000
	s_addc_u32 s5, s65, 0
	v_mov_b32_e32 v4, 1
	s_waitcnt vmcnt(0)
	global_atomic_add v4, v2, v4, s[4:5] offset:1024 sc0
	buffer_inv sc1
	s_waitcnt vmcnt(0)
	v_cvt_f32_u32_e32 v2, v1
	v_rcp_f32_e32 v2, v2
	v_cvt_f32_u32_e32 v5, v4
	v_add_f32_e32 v5, 0.5, v5
	v_mul_f32_e32 v5, v5, v2
	v_cvt_u32_f32_e32 v5, v5
	v_add_u32_e32 v2, 1, v5
	v_mul_lo_u32 v2, v2, v1
	v_add_u32_e32 v4, 1, v4
	v_cmp_ne_u32_e32 vcc, v4, v2
	v_mov_b32_e32 v2, 0
	s_cbranch_vccnz .Lgb0_waittop
	v_mov_b32_e32 v4, 1
	s_add_u32 s4, s64, 0x2400
	s_addc_u32 s5, s65, 0
	global_atomic_add v2, v4, s[4:5] offset:0
	global_atomic_add v2, v4, s[4:5] offset:256
	global_atomic_add v2, v4, s[4:5] offset:512
	global_atomic_add v2, v4, s[4:5] offset:768
	global_atomic_add v2, v4, s[4:5] offset:1024
	global_atomic_add v2, v4, s[4:5] offset:1280
	global_atomic_add v2, v4, s[4:5] offset:1536
	global_atomic_add v2, v4, s[4:5] offset:1792
	global_atomic_add v2, v4, s[4:5] offset:2048
	global_atomic_add v2, v4, s[4:5] offset:2304
	global_atomic_add v2, v4, s[4:5] offset:2560
	global_atomic_add v2, v4, s[4:5] offset:2816
	global_atomic_add v2, v4, s[4:5] offset:3072
	global_atomic_add v2, v4, s[4:5] offset:3328
	global_atomic_add v2, v4, s[4:5] offset:3584
	global_atomic_add v2, v4, s[4:5] offset:3840
	s_branch .Lgb0_exit
.Lgb0_waittop:
	s_add_u32 s4, s0, 0x2000
	s_addc_u32 s5, s1, 0
	s_mov_b32 s7, 0
.Lgb0_t_spin:
	global_load_dword v4, v2, s[4:5] offset:1024 sc1
	s_waitcnt vmcnt(0)
	v_cmp_ne_u32_e32 vcc, v4, v3
	s_cbranch_vccnz .Lgb0_t_done
	s_sleep 1
	s_add_i32 s7, s7, 1
	s_and_b32 s6, s7, 0xff
	s_cmp_lg_u32 s6, 0
	s_cbranch_scc1 .Lgb0_t_spin
	global_load_dword v4, v2, s[64:65] offset:512 sc1
	s_waitcnt vmcnt(0)
	v_cmp_ne_u32_e32 vcc, 0, v4
	s_cbranch_vccnz .Lgb0_t_done
	s_cmp_lt_u32 s7, 0x40001
	s_cbranch_scc1 .Lgb0_t_spin
	v_mov_b32_e32 v4, 1
	global_atomic_add v2, v4, s[64:65] offset:512
.Lgb0_t_done:
.Lgb0_exit:
.LBB0_162:
	s_or_b64 exec, exec, s[2:3]
	s_waitcnt lgkmcnt(0)
	s_barrier

; __device__ __forceinline__ unsigned xb_ld(unsigned* p)              { return __hip_atomic_load(p, __ATOMIC_RELAXED, __HIP_MEMORY_SCOPE_AGENT); }
; __device__ __forceinline__ unsigned xb_add(unsigned* p, unsigned v) { return __hip_atomic_fetch_add(p, v, __ATOMIC_RELAXED, __HIP_MEMORY_SCOPE_AGENT); }
; #define XB_SPIN(cond, bar) do { unsigned _sp = 0; while (cond) { __builtin_amdgcn_s_sleep(1); \
;     if ((++_sp & 255u) == 0u) { if (xb_ld(&(bar)[XB_TMO])) break; if (_sp > XB_SPIN_CAP) { atomicAdd(&(bar)[XB_TMO], 1u); break; } } } } while (0)
; __device__ __forceinline__ void xcd_barrier(const XcdBarrier& b) {
;     ...
;         const unsigned old = xb_add(&bar[XB_XSUB(b.x)], 1u);
;         const unsigned gen = old / nloc;
;         if (old + 1u == (gen + 1u) * nloc) {
;             __builtin_amdgcn_fence(__ATOMIC_RELEASE, "agent");
;             asm volatile("s_waitcnt vmcnt(0)" ::: "memory");
;             const unsigned og = xb_add(&bar[XB_TOP], 1u);
;             const unsigned tg = og / nx;
;             if (og + 1u == (tg + 1u) * nx) xb_add(&bar[XB_TOPGEN], 1u);
;             else XB_SPIN(xb_ld(&bar[XB_TOPGEN]) == tg, bar);
;             __builtin_amdgcn_fence(__ATOMIC_ACQUIRE, "agent");
;             xb_add(&bar[XB_XGEN(b.x)], 1u);
;             asm volatile("s_waitcnt vmcnt(0)" ::: "memory");
;         } else {
;             XB_SPIN(xb_ld(&bar[XB_XGEN(b.x)]) == gen, bar);
;             __builtin_amdgcn_fence(__ATOMIC_ACQUIRE, "agent");
;             asm volatile("s_waitcnt vmcnt(0)" ::: "memory");
;         }
.Lgb1_leader:
	buffer_wbl2 sc1
	v_mov_b32_e32 v3, v5
	s_add_u32 s6, s64, 0x3000
	s_addc_u32 s7, s65, 0
	v_mov_b32_e32 v4, 1
	s_waitcnt vmcnt(0)
	global_atomic_add v4, v2, v4, s[6:7] offset:1024 sc0
	buffer_inv sc1
	s_waitcnt vmcnt(0)
	v_cvt_f32_u32_e32 v2, v1
	v_rcp_f32_e32 v2, v2
	v_cvt_f32_u32_e32 v5, v4
	v_add_f32_e32 v5, 0.5, v5
	v_mul_f32_e32 v5, v5, v2
	v_cvt_u32_f32_e32 v5, v5
	v_add_u32_e32 v2, 1, v5
	v_mul_lo_u32 v2, v2, v1
	v_add_u32_e32 v4, 1, v4
	v_cmp_ne_u32_e32 vcc, v4, v2
	v_mov_b32_e32 v2, 0
	s_cbranch_vccnz .Lgb1_waittop
	v_mov_b32_e32 v4, 1
	s_add_u32 s6, s64, 0x2400
	s_addc_u32 s7, s65, 0
	global_atomic_add v2, v4, s[6:7] offset:0
	global_atomic_add v2, v4, s[6:7] offset:256
	global_atomic_add v2, v4, s[6:7] offset:512
	global_atomic_add v2, v4, s[6:7] offset:768
	global_atomic_add v2, v4, s[6:7] offset:1024
	global_atomic_add v2, v4, s[6:7] offset:1280
	global_atomic_add v2, v4, s[6:7] offset:1536
	global_atomic_add v2, v4, s[6:7] offset:1792
	global_atomic_add v2, v4, s[6:7] offset:2048
	global_atomic_add v2, v4, s[6:7] offset:2304
	global_atomic_add v2, v4, s[6:7] offset:2560
	global_atomic_add v2, v4, s[6:7] offset:2816
	global_atomic_add v2, v4, s[6:7] offset:3072
	global_atomic_add v2, v4, s[6:7] offset:3328
	global_atomic_add v2, v4, s[6:7] offset:3584
	global_atomic_add v2, v4, s[6:7] offset:3840
	s_branch .Lgb1_exit
.Lgb1_waittop:
	s_add_u32 s6, s0, 0x2000
	s_addc_u32 s7, s1, 0
	s_mov_b32 s9, 0
.Lgb1_t_spin:
	global_load_dword v4, v2, s[6:7] offset:1024 sc1
	s_waitcnt vmcnt(0)
	v_cmp_ne_u32_e32 vcc, v4, v3
	s_cbranch_vccnz .Lgb1_t_done
	s_sleep 1
	s_add_i32 s9, s9, 1
	s_and_b32 s8, s9, 0xff
	s_cmp_lg_u32 s8, 0
	s_cbranch_scc1 .Lgb1_t_spin
	global_load_dword v4, v2, s[64:65] offset:512 sc1
	s_waitcnt vmcnt(0)
	v_cmp_ne_u32_e32 vcc, 0, v4
	s_cbranch_vccnz .Lgb1_t_done
	s_cmp_lt_u32 s9, 0x40001
	s_cbranch_scc1 .Lgb1_t_spin
	v_mov_b32_e32 v4, 1
	global_atomic_add v2, v4, s[64:65] offset:512
.Lgb1_t_done:
.Lgb1_exit:
.LBB0_345:
	s_or_b64 exec, exec, s[4:5]
	s_waitcnt lgkmcnt(0)
	s_barrier

; __device__ __forceinline__ unsigned xb_ld(unsigned* p)              { return __hip_atomic_load(p, __ATOMIC_RELAXED, __HIP_MEMORY_SCOPE_AGENT); }
; __device__ __forceinline__ unsigned xb_add(unsigned* p, unsigned v) { return __hip_atomic_fetch_add(p, v, __ATOMIC_RELAXED, __HIP_MEMORY_SCOPE_AGENT); }
; #define XB_SPIN(cond, bar) do { unsigned _sp = 0; while (cond) { __builtin_amdgcn_s_sleep(1); \
;     if ((++_sp & 255u) == 0u) { if (xb_ld(&(bar)[XB_TMO])) break; if (_sp > XB_SPIN_CAP) { atomicAdd(&(bar)[XB_TMO], 1u); break; } } } } while (0)
; __device__ __forceinline__ void xcd_barrier(const XcdBarrier& b) {
;     ...
;             __builtin_amdgcn_fence(__ATOMIC_ACQUIRE, "agent");
;             xb_add(&bar[XB_XGEN(b.x)], 1u);
;             asm volatile("s_waitcnt vmcnt(0)" ::: "memory");
;         } else {
;             XB_SPIN(xb_ld(&bar[XB_XGEN(b.x)]) == gen, bar);
;             __builtin_amdgcn_fence(__ATOMIC_ACQUIRE, "agent");
;             asm volatile("s_waitcnt vmcnt(0)" ::: "memory");
;         }
;     }
;     __syncthreads();
; __device__ __forceinline__ void p11b_weights(const Params& P, int tid, int vb) {
;     const _Float16* PART = (const _Float16*)(P.ws + WS_PART); const float* GATE = (const float*)(P.ws + WS_GATE); const float* SSQ1 = (const float*)(P.ws + WS_SSQ1);
;     unsigned char* REC = P.ws + WS_REC; const float* SUR = (const float*)(P.ws + WS_SUR); const float* SVR = (const float*)(P.ws + WS_SVR);
;     const size_t n = (size_t)NTOK * 32, st = (size_t)gridDim.x * 512;
;     for (size_t i = (size_t)vb * 512 + tid; i < n; i += 2 * st) {
;         WIn a, b; p11b_load(a, SUR, SVR, GATE, PART, SSQ1, i); const bool hb = i + st < n; if (hb) p11b_load(b, SUR, SVR, GATE, PART, SSQ1, i + st);
;         p11b_finish(a, REC, i); if (hb) p11b_finish(b, REC, i + st);
;     }
.Lgb9_t_done:
.Lgb9_exit:
.LBB0_1413:
	s_or_b64 exec, exec, s[2:3]
	v_mov_b32_e32 v2, v0
	s_ashr_i32 s73, s72, 31
	s_waitcnt lgkmcnt(0)
	s_barrier
	s_lshl_b64 s[0:1], s[72:73], 9
	v_ashrrev_i32_e32 v3, 31, v2
	v_lshl_add_u64 v[38:39], s[0:1], 0, v[2:3]
	s_mov_b64 s[4:5], 0x100000
	v_cmp_gt_u64_e32 vcc, s[4:5], v[38:39]
	s_and_saveexec_b64 s[6:7], vcc
	s_cbranch_execz .LBB0_1452
	s_add_u32 s12, s64, 0x17800000
	s_addc_u32 s13, s65, 0
	s_add_u32 s14, s64, 0xa800000
	s_addc_u32 s15, s65, 0
	s_add_u32 s16, s64, 0x1fac0000
	s_addc_u32 s17, s65, 0
	s_add_u32 s22, s64, 0xd800000
	s_addc_u32 s23, s65, 0
	s_add_u32 s24, s64, 0xf000000
	s_addc_u32 s25, s65, 0
	s_add_u32 s26, s64, 0x10000000
	s_mov_b32 s69, 0
	s_addc_u32 s27, s65, 0
	s_lshl_b64 s[30:31], s[68:69], 11
	s_lshl_b64 s[0:1], s[72:73], 11
	s_lshl_b64 s[28:29], s[68:69], 9
	v_lshl_add_u64 v[26:27], v[2:3], 2, s[0:1]
	s_lshl_b64 s[34:35], s[68:69], 12
	s_mov_b64 s[36:37], 0
	v_mov_b32_e32 v29, 0
	v_mov_b32_e32 v1, 0x358637bd
	s_mov_b32 s21, 0x800000
	s_mov_b32 s31, 0x378e98ab
	s_mov_b32 s45, 0x3b7cd369
	s_mov_b32 s46, 0xbcc618b2
	s_mov_b32 s47, 0x3dda74e4
	s_mov_b32 s48, 0x3f228afd
	s_mov_b32 s49, 0x3e03c728
	s_mov_b32 s50, 0xbfb8aa3b
	s_mov_b32 s51, 0x42ce8ed0
	s_mov_b32 s52, 0xc2b17218
	v_mov_b32_e32 v52, 0x3ba10414
	s_brev_b32 s53, -2
	s_movk_i32 s54, 0x300
	s_mov_b64 s[38:39], 0xfffff
	v_mov_b32_e32 v53, 0xb9c68948
	v_mov_b32_e32 v54, 0x7f800000
	s_branch .LBB0_1417

; #define LAS __attribute__((address_space(3)))
; __device__ __forceinline__ unsigned xb_ld(unsigned* p)              { return __hip_atomic_load(p, __ATOMIC_RELAXED, __HIP_MEMORY_SCOPE_AGENT); }
; __device__ __forceinline__ void xcd_barrier(const XcdBarrier& b) {
;     ...
;             __builtin_amdgcn_fence(__ATOMIC_ACQUIRE, "agent");
;             xb_add(&bar[XB_XGEN(b.x)], 1u);
;             asm volatile("s_waitcnt vmcnt(0)" ::: "memory");
;         } else {
;             XB_SPIN(xb_ld(&bar[XB_XGEN(b.x)]) == gen, bar);
;             __builtin_amdgcn_fence(__ATOMIC_ACQUIRE, "agent");
;             asm volatile("s_waitcnt vmcnt(0)" ::: "memory");
;         }
;     }
;     __syncthreads();
; __device__ __forceinline__ void p11c_vacc(const Params& P, LAS unsigned char* lds, int lane, int wave, int vb) {
;     const unsigned char* V4 = P.ws + WS_V4; const unsigned char* REC = P.ws + WS_REC;
;     bf16* XB = (bf16*)(P.ws + WS_HN); float* SSQ = (float*)(P.ws + WS_SSQ);
;     const int x = vb & 3, wgx = vb >> 2, nwg = gridDim.x >> 2, rg = lane >> 3, ch = lane & 7, n16 = lane & 15, kb = lane >> 4;
;     const int tstep = nwg * NW;
;     LAS unsigned char* vbuf = lds + wave * 16384;
;     LAS unsigned char* ring = lds + 131072 + wave * 2304;
;     const unsigned char* tbl = V4 + (size_t)x * 2097152 + 16 * ch;
;     LAS unsigned char* wr0 = vbuf + rg * 128 + ((ch ^ ((rg >> 1) & 7)) << 4); LAS unsigned char* wr1 = vbuf + rg * 128 + ((ch ^ ((4 + (rg >> 1)) & 7)) << 4);
;     const unsigned swr = (unsigned)(n16 >> 1) & 7u;
;     const LAS unsigned char* rdb = vbuf + (kb * 32 + n16) * 128;
;     const bool pl = (n16 & 3) < 2;
;     const int D = 32 * (n16 >> 1) + 8 * (2 * (kb & 1) + (n16 & 1));
;     VCtx C{tbl, REC, wr0, wr1, rdb, ring, swr, rg, n16, kb, lane, pl};
;     const int t0 = wgx * NW + wave;
;     v4u vdA[16], vdB[16], rraw = {0u, 0u, 0u, 0u};
;     { v4u r0 = {0u, 0u, 0u, 0u}, r1 = {0u, 0u, 0u, 0u};
;       if (lane < 48) { r0 = *(const v4u*)(REC + (size_t)t0 * 768 + 16 * lane); r1 = *(const v4u*)(REC + (size_t)(t0 + tstep) * 768 + 16 * lane); rraw = *(const v4u*)(REC + (size_t)(t0 + 2 * tstep) * 768 + 16 * lane);
;           *(LAS v4u*)(ring + 16 * lane) = r0; *(LAS v4u*)(ring + 768 + 16 * lane) = r1; }
;       asm volatile("s_waitcnt lgkmcnt(0)" ::: "memory");
.Lgb10_t_done:
.Lgb10_exit:
.LBB0_1504:
	s_or_b64 exec, exec, s[2:3]
	v_mov_b32_e32 v134, v0
	s_add_u32 s12, s64, 0xd800000
	s_mul_i32 s0, s70, 0x900
	s_waitcnt lgkmcnt(0)
	s_barrier
	s_addc_u32 s13, s65, 0
	v_and_b32_e32 v135, 63, v134
	s_add_i32 s21, s0, 0
	v_mov_b32_e32 v2, 0
	s_add_i32 s21, s21, 0x20000
	v_cmp_lt_u32_e64 s[2:3], 47, v135
	v_cmp_gt_u32_e64 s[4:5], 48, v135
	v_mov_b32_e32 v3, v2
	v_mov_b32_e32 v4, v2
	v_mov_b32_e32 v5, v2
	v_lshlrev_b32_e32 v138, 4, v135
	s_and_saveexec_b64 s[6:7], s[4:5]
	s_cbranch_execz .LBB0_1506
	s_add_u32 s0, s12, s43
	s_addc_u32 s1, s13, s42
	s_add_i32 s16, s20, s11
	s_mul_i32 s14, s16, 0x300
	s_mul_hi_i32 s15, s16, 0x300
	s_add_u32 s14, s12, s14
	s_addc_u32 s15, s13, s15
	global_load_dwordx4 v[6:9], v138, s[0:1]
	global_load_dwordx4 v[10:13], v138, s[14:15]
	s_add_i32 s0, s16, s11
	s_mul_hi_i32 s1, s0, 0x300
	s_mulk_i32 s0, 0x300
	s_add_u32 s0, s12, s0
	s_addc_u32 s1, s13, s1
	global_load_dwordx4 v[2:5], v138, s[0:1]
	v_add_u32_e32 v1, s21, v138
	s_waitcnt vmcnt(2)
	ds_write_b128 v1, v[6:9]
	s_waitcnt vmcnt(1)
	ds_write_b128 v1, v[10:13] offset:768

; __device__ __forceinline__ unsigned xb_ld(unsigned* p)              { return __hip_atomic_load(p, __ATOMIC_RELAXED, __HIP_MEMORY_SCOPE_AGENT); }
; __device__ __forceinline__ unsigned xb_add(unsigned* p, unsigned v) { return __hip_atomic_fetch_add(p, v, __ATOMIC_RELAXED, __HIP_MEMORY_SCOPE_AGENT); }
; #define XB_SPIN(cond, bar) do { unsigned _sp = 0; while (cond) { __builtin_amdgcn_s_sleep(1); \
;     if ((++_sp & 255u) == 0u) { if (xb_ld(&(bar)[XB_TMO])) break; if (_sp > XB_SPIN_CAP) { atomicAdd(&(bar)[XB_TMO], 1u); break; } } } } while (0)
; __device__ __forceinline__ void xcd_barrier(const XcdBarrier& b) {
;     ...
;         const unsigned old = xb_add(&bar[XB_XSUB(b.x)], 1u);
;         const unsigned gen = old / nloc;
;         if (old + 1u == (gen + 1u) * nloc) {
;             __builtin_amdgcn_fence(__ATOMIC_RELEASE, "agent");
;             asm volatile("s_waitcnt vmcnt(0)" ::: "memory");
;             const unsigned og = xb_add(&bar[XB_TOP], 1u);
;             const unsigned tg = og / nx;
;             if (og + 1u == (tg + 1u) * nx) xb_add(&bar[XB_TOPGEN], 1u);
;             else XB_SPIN(xb_ld(&bar[XB_TOPGEN]) == tg, bar);
;             __builtin_amdgcn_fence(__ATOMIC_ACQUIRE, "agent");
;             xb_add(&bar[XB_XGEN(b.x)], 1u);
;             asm volatile("s_waitcnt vmcnt(0)" ::: "memory");
;         } else {
;             XB_SPIN(xb_ld(&bar[XB_XGEN(b.x)]) == gen, bar);
;             __builtin_amdgcn_fence(__ATOMIC_ACQUIRE, "agent");
;             asm volatile("s_waitcnt vmcnt(0)" ::: "memory");
;         }
.Lgb12_leader:
	buffer_wbl2 sc1
	v_mov_b32_e32 v2, v4
	s_add_u32 s8, s64, 0x3000
	s_addc_u32 s9, s65, 0
	v_mov_b32_e32 v3, 1
	s_waitcnt vmcnt(0)
	global_atomic_add v3, v1, v3, s[8:9] offset:1024 sc0
	buffer_inv sc1
	s_waitcnt vmcnt(0)
	v_cvt_f32_u32_e32 v1, v0
	v_rcp_f32_e32 v1, v1
	v_cvt_f32_u32_e32 v4, v3
	v_add_f32_e32 v4, 0.5, v4
	v_mul_f32_e32 v4, v4, v1
	v_cvt_u32_f32_e32 v4, v4
	v_add_u32_e32 v1, 1, v4
	v_mul_lo_u32 v1, v1, v0
	v_add_u32_e32 v3, 1, v3
	v_cmp_ne_u32_e32 vcc, v3, v1
	v_mov_b32_e32 v1, 0
	s_cbranch_vccnz .Lgb12_waittop
	v_mov_b32_e32 v3, 1
	s_add_u32 s8, s64, 0x2400
	s_addc_u32 s9, s65, 0
	global_atomic_add v1, v3, s[8:9] offset:0
	global_atomic_add v1, v3, s[8:9] offset:256
	global_atomic_add v1, v3, s[8:9] offset:512
	global_atomic_add v1, v3, s[8:9] offset:768
	global_atomic_add v1, v3, s[8:9] offset:1024
	global_atomic_add v1, v3, s[8:9] offset:1280
	global_atomic_add v1, v3, s[8:9] offset:1536
	global_atomic_add v1, v3, s[8:9] offset:1792
	global_atomic_add v1, v3, s[8:9] offset:2048
	global_atomic_add v1, v3, s[8:9] offset:2304
	global_atomic_add v1, v3, s[8:9] offset:2560
	global_atomic_add v1, v3, s[8:9] offset:2816
	global_atomic_add v1, v3, s[8:9] offset:3072
	global_atomic_add v1, v3, s[8:9] offset:3328
	global_atomic_add v1, v3, s[8:9] offset:3584
	global_atomic_add v1, v3, s[8:9] offset:3840
	s_branch .Lgb12_exit
.Lgb12_waittop:
	s_add_u32 s8, s0, 0x2000
	s_addc_u32 s9, s1, 0
	s_mov_b32 s11, 0
.Lgb12_t_spin:
	global_load_dword v3, v1, s[8:9] offset:1024 sc1
	s_waitcnt vmcnt(0)
	v_cmp_ne_u32_e32 vcc, v3, v2
	s_cbranch_vccnz .Lgb12_t_done
	s_sleep 1
	s_add_i32 s11, s11, 1
	s_and_b32 s10, s11, 0xff
	s_cmp_lg_u32 s10, 0
	s_cbranch_scc1 .Lgb12_t_spin
	global_load_dword v3, v1, s[64:65] offset:512 sc1
	s_waitcnt vmcnt(0)
	v_cmp_ne_u32_e32 vcc, 0, v3
	s_cbranch_vccnz .Lgb12_t_done
	s_cmp_lt_u32 s11, 0x40001
	s_cbranch_scc1 .Lgb12_t_spin
	v_mov_b32_e32 v3, 1
	global_atomic_add v1, v3, s[64:65] offset:512
.Lgb12_t_done:
.Lgb12_exit:
.LBB0_1735:
	s_or_b64 exec, exec, s[6:7]
	s_waitcnt lgkmcnt(0)
	s_barrier
